# v38 + SSM-matrix prep split three ways onto workgroups that carry no int8 weight task (g and the top 64 prep workgroups)
# baseline (speedup 1.0000x reference)
.LBB0_1411:
	s_cmp_eq_u32 s76, 3
	s_cbranch_scc1 .LBB0_1587
	v_readlane_b32 s0, v254, 47
	v_readlane_b32 s2, v253, 27
	v_readlane_b32 s3, v253, 28
	v_mov_b32_e32 v1, s0
	ds_read_b32 v1, v1
	s_waitcnt lgkmcnt(0)
	s_barrier
	v_readfirstlane_b32 s0, v1
	s_lshl_b32 s0, s0, 2
	s_ashr_i32 s1, s0, 31
	s_abs_i32 s0, s0
	s_mul_hi_u32 s2, s0, s2
	s_mul_i32 s2, s2, s3
	s_sub_i32 s0, s0, s2
	s_sub_i32 s2, s0, s3
	s_cmp_ge_u32 s0, s3
	s_cselect_b32 s0, s2, s0
	s_sub_i32 s2, s0, s3
	s_cmp_ge_u32 s0, s3
	s_cselect_b32 s0, s2, s0
	s_xor_b32 s0, s0, s1
	s_sub_i32 s0, s0, s1
	s_cmp_lt_i32 s88, s0
	s_cbranch_scc1 .LBB0_1587
	s_sub_i32 s45, s88, s0
	s_sub_i32 s33, s78, s0
	v_readlane_b32 s0, v253, 61
	v_mov_b32_e32 v22, v232
	v_readlane_b32 s4, v253, 63
	v_mov_b32_e32 v2, s0
	ds_read_b64 v[4:5], v2
	v_readlane_b32 s0, v253, 62
	v_readlane_b32 s8, v254, 0
	v_readlane_b32 s12, v254, 1
	v_mov_b32_e32 v2, s0
	s_waitcnt lgkmcnt(0)
	v_readfirstlane_b32 s21, v5
	v_readfirstlane_b32 s20, v4
	ds_read_b128 v[4:7], v2
	v_mov_b32_e32 v2, s4
	s_add_i32 s92, s76, 1
	v_ashrrev_i32_e32 v1, 6, v22
	v_and_b32_e32 v23, 63, v22
	s_waitcnt lgkmcnt(0)
	v_readfirstlane_b32 s1, v5
	v_readfirstlane_b32 s3, v4
	v_readfirstlane_b32 s0, v7
	v_readfirstlane_b32 s2, v6
	ds_read_b128 v[4:7], v2
	v_mov_b32_e32 v2, s8
	v_readfirstlane_b32 s44, v1
	s_waitcnt lgkmcnt(0)
	v_readfirstlane_b32 s5, v5
	v_readfirstlane_b32 s7, v4
	v_readfirstlane_b32 s4, v7
	v_readfirstlane_b32 s6, v6
	ds_read_b128 v[4:7], v2
	v_mov_b32_e32 v2, s12
	s_waitcnt lgkmcnt(0)
	v_readfirstlane_b32 s9, v5
	v_readfirstlane_b32 s11, v4
	ds_read_b64 v[4:5], v2
	v_readfirstlane_b32 s8, v7
	v_readfirstlane_b32 s10, v6
	s_waitcnt lgkmcnt(0)
	v_readfirstlane_b32 s12, v5
	v_readfirstlane_b32 s13, v4
	s_cmp_gt_i32 s33, 159
	s_cbranch_scc0 .Ls3_tb
	s_cmp_lt_i32 s45, 32
	s_cbranch_scc1 .Ls3_job
	s_sub_i32 s14, s45, s33
	s_add_i32 s14, s14, 64
	s_cmp_gt_i32 s14, -1
	s_cbranch_scc1 .Ls3_job
	s_cmp_eq_u32 s45, s45
	s_branch .Ls3_td
.Ls3_tb:
	s_cmp_gt_i32 s33, 127
	s_cselect_b32 s14, 127, 31
	s_cmp_gt_i32 s45, s14
	s_branch .Ls3_td
.Ls3_job:
	s_cmp_lg_u32 s45, s45
.Ls3_td:
	s_cbranch_scc1 .LBB0_1459
	s_lshl_b64 s[14:15], s[92:93], 13
	s_add_u32 s18, s3, s14
	s_addc_u32 s19, s1, s15
	s_add_u32 s22, s2, s14
	s_addc_u32 s23, s0, s15
	s_lshl_b32 s0, s92, 5
	s_mov_b32 s1, s93
	s_lshl_b64 s[0:1], s[0:1], 2
	s_add_u32 s46, s7, s0
	s_addc_u32 s47, s5, s1
	s_lshl_b64 s[0:1], s[92:93], 17
	s_add_u32 s24, s6, s0
	s_addc_u32 s25, s4, s1
	s_add_u32 s26, s11, s0
	s_addc_u32 s27, s9, s1
	s_add_u32 s28, s10, s0
	s_addc_u32 s29, s8, s1
	s_add_u32 s30, s13, s0
	s_addc_u32 s31, s12, s1
	s_movk_i32 s0, 0x440
	v_cmp_gt_i32_e64 s[2:3], s0, v22
	s_movk_i32 s0, 0x400
	s_add_u32 s48, s20, 0x27e0000
	v_cmp_gt_i32_e64 s[4:5], s0, v22
	s_movk_i32 s0, 0x1000
	s_addc_u32 s49, s21, 0
	v_cmp_gt_i32_e64 s[6:7], s0, v22
	s_add_u32 s50, s20, 0x23e0000
	s_mov_b32 s0, 0xc000
	s_addc_u32 s51, s21, 0
	v_cmp_gt_i32_e64 s[8:9], s0, v22
	s_mov_b32 s0, 0x8000
	v_cmp_gt_i32_e64 s[10:11], s0, v22
	s_add_u32 s34, s20, 0x1100000
	v_lshlrev_b32_e32 v2, 3, v22
	v_and_b32_e32 v4, 15, v22
	v_readlane_b32 s0, v254, 2
	v_cmp_gt_i32_e64 s[12:13], 64, v22
	s_addc_u32 s35, s21, 0
	v_add_u32_e32 v12, 0, v2
	v_add_u32_e32 v13, s0, v2
	s_lshl_b32 s52, s45, 10
	s_lshl_b32 s53, s33, 10
	v_lshlrev_b32_e32 v14, 2, v22
	v_lshl_add_u32 v15, v4, 3, s0
	v_lshlrev_b32_e32 v16, 1, v22
	s_cmp_gt_i32 s33, 159
	s_cbranch_scc0 .Ls3_four
	s_cmp_lt_i32 s45, 32
	s_cbranch_scc0 .Ls3_hi
	s_mov_b32 s36, s45
	s_mov_b32 s0, 0
	s_branch .Ls3_set
.Ls3_hi:
	s_sub_i32 s0, s45, s33
	s_add_i32 s0, s0, 64
	s_and_b32 s36, s0, 31
	s_lshr_b32 s0, s0, 5
	s_add_i32 s0, s0, 1
.Ls3_set:
	s_lshl_b32 s52, s36, 10
	s_lshl_b32 s1, s0, 14
	v_mov_b32_e32 v138, s1
	s_lshl_b32 s1, s1, 1
	v_mov_b32_e32 v137, s1
	v_add_u32_e32 v135, 0x3dff, v138
	s_mul_i32 s1, s0, 0x2a00
	s_cmp_lg_u32 s0, 0
	s_cselect_b32 s37, 0x200, 0
	s_add_i32 s1, s1, s37
	v_mov_b32_e32 v140, s1
	s_lshl_b32 s1, s1, 1
	v_mov_b32_e32 v139, s1
	s_add_i32 s1, s0, 1
	s_mul_i32 s1, s1, 0x2a00
	s_add_i32 s1, s1, -1
	v_mov_b32_e32 v136, s1
	s_branch .LBB0_1416
.Ls3_four:
	s_cmp_gt_i32 s33, 127
	s_cbranch_scc1 .Ls3_four_go
	s_mov_b32 s36, s45
	v_mov_b32_e32 v135, 0xbdff
	v_mov_b32_e32 v136, 0x7dff
	v_mov_b32_e32 v137, 0
	v_mov_b32_e32 v138, 0
	v_mov_b32_e32 v139, 0
	v_mov_b32_e32 v140, 0
	s_branch .LBB0_1416
